# P4 state scan: 64 dependent steps per thread now run with 32 chunk loads in flight (saddr addressing, loads-only counted waits) instead of 2
# speedup vs baseline: 1.0128x; 1.0011x over previous
.LBB0_871:
	v_lshlrev_b32_e32 v78, 3, v1
	v_lshlrev_b32_e32 v79, 2, v1
	s_add_u32 s98, s6, 0xff900000
	s_addc_u32 s99, s7, -1
	s_mov_b32 s100, s4
	s_mov_b32 s101, s5
	global_load_dwordx2 v[14:15], v78, s[98:99]
	s_add_u32 s98, s98, 0x100000
	s_addc_u32 s99, s99, 0
	global_load_dwordx2 v[16:17], v78, s[98:99]
	s_add_u32 s98, s98, 0x100000
	s_addc_u32 s99, s99, 0
	global_load_dwordx2 v[18:19], v78, s[98:99]
	s_add_u32 s98, s98, 0x100000
	s_addc_u32 s99, s99, 0
	global_load_dwordx2 v[20:21], v78, s[98:99]
	s_add_u32 s98, s98, 0x100000
	s_addc_u32 s99, s99, 0
	global_load_dwordx2 v[22:23], v78, s[98:99]
	s_add_u32 s98, s98, 0x100000
	s_addc_u32 s99, s99, 0
	global_load_dwordx2 v[24:25], v78, s[98:99]
	s_add_u32 s98, s98, 0x100000
	s_addc_u32 s99, s99, 0
	global_load_dwordx2 v[26:27], v78, s[98:99]
	s_add_u32 s98, s98, 0x100000
	s_addc_u32 s99, s99, 0
	global_load_dwordx2 v[28:29], v78, s[98:99]
	s_add_u32 s98, s98, 0x100000
	s_addc_u32 s99, s99, 0
	global_load_dwordx2 v[30:31], v78, s[98:99]
	s_add_u32 s98, s98, 0x100000
	s_addc_u32 s99, s99, 0
	global_load_dwordx2 v[32:33], v78, s[98:99]
	s_add_u32 s98, s98, 0x100000
	s_addc_u32 s99, s99, 0
	global_load_dwordx2 v[34:35], v78, s[98:99]
	s_add_u32 s98, s98, 0x100000
	s_addc_u32 s99, s99, 0
	global_load_dwordx2 v[36:37], v78, s[98:99]
	s_add_u32 s98, s98, 0x100000
	s_addc_u32 s99, s99, 0
	global_load_dwordx2 v[38:39], v78, s[98:99]
	s_add_u32 s98, s98, 0x100000
	s_addc_u32 s99, s99, 0
	global_load_dwordx2 v[40:41], v78, s[98:99]
	s_add_u32 s98, s98, 0x100000
	s_addc_u32 s99, s99, 0
	global_load_dwordx2 v[42:43], v78, s[98:99]
	s_add_u32 s98, s98, 0x100000
	s_addc_u32 s99, s99, 0
	global_load_dwordx2 v[44:45], v78, s[98:99]
	s_add_u32 s98, s98, 0x100000
	s_addc_u32 s99, s99, 0
	global_load_dwordx2 v[46:47], v78, s[98:99]
	s_add_u32 s98, s98, 0x100000
	s_addc_u32 s99, s99, 0
	global_load_dwordx2 v[48:49], v78, s[98:99]
	s_add_u32 s98, s98, 0x100000
	s_addc_u32 s99, s99, 0
	global_load_dwordx2 v[50:51], v78, s[98:99]
	s_add_u32 s98, s98, 0x100000
	s_addc_u32 s99, s99, 0
	global_load_dwordx2 v[52:53], v78, s[98:99]
	s_add_u32 s98, s98, 0x100000
	s_addc_u32 s99, s99, 0
	global_load_dwordx2 v[54:55], v78, s[98:99]
	s_add_u32 s98, s98, 0x100000
	s_addc_u32 s99, s99, 0
	global_load_dwordx2 v[56:57], v78, s[98:99]
	s_add_u32 s98, s98, 0x100000
	s_addc_u32 s99, s99, 0
	global_load_dwordx2 v[58:59], v78, s[98:99]
	s_add_u32 s98, s98, 0x100000
	s_addc_u32 s99, s99, 0
	global_load_dwordx2 v[60:61], v78, s[98:99]
	s_add_u32 s98, s98, 0x100000
	s_addc_u32 s99, s99, 0
	global_load_dwordx2 v[62:63], v78, s[98:99]
	s_add_u32 s98, s98, 0x100000
	s_addc_u32 s99, s99, 0
	global_load_dwordx2 v[64:65], v78, s[98:99]
	s_add_u32 s98, s98, 0x100000
	s_addc_u32 s99, s99, 0
	global_load_dwordx2 v[66:67], v78, s[98:99]
	s_add_u32 s98, s98, 0x100000
	s_addc_u32 s99, s99, 0
	global_load_dwordx2 v[68:69], v78, s[98:99]
	s_add_u32 s98, s98, 0x100000
	s_addc_u32 s99, s99, 0
	global_load_dwordx2 v[70:71], v78, s[98:99]
	s_add_u32 s98, s98, 0x100000
	s_addc_u32 s99, s99, 0
	global_load_dwordx2 v[72:73], v78, s[98:99]
	s_add_u32 s98, s98, 0x100000
	s_addc_u32 s99, s99, 0
	global_load_dwordx2 v[74:75], v78, s[98:99]
	s_add_u32 s98, s98, 0x100000
	s_addc_u32 s99, s99, 0
	global_load_dwordx2 v[76:77], v78, s[98:99]
	s_add_u32 s98, s98, 0x100000
	s_addc_u32 s99, s99, 0
	s_waitcnt vmcnt(31)
	v_cvt_pk_bf16_f32 v80, v8, v9
	v_pk_fma_f32 v[8:9], v[4:5], v[8:9], v[14:15]
	global_store_dword v79, v80, s[100:101]
	s_add_u32 s100, s100, 0x80000
	s_addc_u32 s101, s101, 0
	global_load_dwordx2 v[14:15], v78, s[98:99]
	s_add_u32 s98, s98, 0x100000
	s_addc_u32 s99, s99, 0
	s_waitcnt vmcnt(31)
	v_cvt_pk_bf16_f32 v81, v8, v9
	v_pk_fma_f32 v[8:9], v[4:5], v[8:9], v[16:17]
	global_store_dword v79, v81, s[100:101]
	s_add_u32 s100, s100, 0x80000
	s_addc_u32 s101, s101, 0
	global_load_dwordx2 v[16:17], v78, s[98:99]
	s_add_u32 s98, s98, 0x100000
	s_addc_u32 s99, s99, 0
	s_waitcnt vmcnt(31)
	v_cvt_pk_bf16_f32 v82, v8, v9
	v_pk_fma_f32 v[8:9], v[4:5], v[8:9], v[18:19]
	global_store_dword v79, v82, s[100:101]
	s_add_u32 s100, s100, 0x80000
	s_addc_u32 s101, s101, 0
	global_load_dwordx2 v[18:19], v78, s[98:99]
	s_add_u32 s98, s98, 0x100000
	s_addc_u32 s99, s99, 0
	s_waitcnt vmcnt(31)
	v_cvt_pk_bf16_f32 v83, v8, v9
	v_pk_fma_f32 v[8:9], v[4:5], v[8:9], v[20:21]
	global_store_dword v79, v83, s[100:101]
	s_add_u32 s100, s100, 0x80000
	s_addc_u32 s101, s101, 0
	global_load_dwordx2 v[20:21], v78, s[98:99]
	s_add_u32 s98, s98, 0x100000
	s_addc_u32 s99, s99, 0
	s_waitcnt vmcnt(31)
	v_cvt_pk_bf16_f32 v80, v8, v9
	v_pk_fma_f32 v[8:9], v[4:5], v[8:9], v[22:23]
	global_store_dword v79, v80, s[100:101]
	s_add_u32 s100, s100, 0x80000
	s_addc_u32 s101, s101, 0
	global_load_dwordx2 v[22:23], v78, s[98:99]
	s_add_u32 s98, s98, 0x100000
	s_addc_u32 s99, s99, 0
	s_waitcnt vmcnt(31)
	v_cvt_pk_bf16_f32 v81, v8, v9
	v_pk_fma_f32 v[8:9], v[4:5], v[8:9], v[24:25]
	global_store_dword v79, v81, s[100:101]
	s_add_u32 s100, s100, 0x80000
	s_addc_u32 s101, s101, 0
	global_load_dwordx2 v[24:25], v78, s[98:99]
	s_add_u32 s98, s98, 0x100000
	s_addc_u32 s99, s99, 0
	s_waitcnt vmcnt(31)
	v_cvt_pk_bf16_f32 v82, v8, v9
	v_pk_fma_f32 v[8:9], v[4:5], v[8:9], v[26:27]
	global_store_dword v79, v82, s[100:101]
	s_add_u32 s100, s100, 0x80000
	s_addc_u32 s101, s101, 0
	global_load_dwordx2 v[26:27], v78, s[98:99]
	s_add_u32 s98, s98, 0x100000
	s_addc_u32 s99, s99, 0
	s_waitcnt vmcnt(31)
	v_cvt_pk_bf16_f32 v83, v8, v9
	v_pk_fma_f32 v[8:9], v[4:5], v[8:9], v[28:29]
	global_store_dword v79, v83, s[100:101]
	s_add_u32 s100, s100, 0x80000
	s_addc_u32 s101, s101, 0
	global_load_dwordx2 v[28:29], v78, s[98:99]
	s_add_u32 s98, s98, 0x100000
	s_addc_u32 s99, s99, 0
	s_waitcnt vmcnt(31)
	v_cvt_pk_bf16_f32 v80, v8, v9
	v_pk_fma_f32 v[8:9], v[4:5], v[8:9], v[30:31]
	global_store_dword v79, v80, s[100:101]
	s_add_u32 s100, s100, 0x80000
	s_addc_u32 s101, s101, 0
	global_load_dwordx2 v[30:31], v78, s[98:99]
	s_add_u32 s98, s98, 0x100000
	s_addc_u32 s99, s99, 0
	s_waitcnt vmcnt(31)
	v_cvt_pk_bf16_f32 v81, v8, v9
	v_pk_fma_f32 v[8:9], v[4:5], v[8:9], v[32:33]
	global_store_dword v79, v81, s[100:101]
	s_add_u32 s100, s100, 0x80000
	s_addc_u32 s101, s101, 0
	global_load_dwordx2 v[32:33], v78, s[98:99]
	s_add_u32 s98, s98, 0x100000
	s_addc_u32 s99, s99, 0
	s_waitcnt vmcnt(31)
	v_cvt_pk_bf16_f32 v82, v8, v9
	v_pk_fma_f32 v[8:9], v[4:5], v[8:9], v[34:35]
	global_store_dword v79, v82, s[100:101]
	s_add_u32 s100, s100, 0x80000
	s_addc_u32 s101, s101, 0
	global_load_dwordx2 v[34:35], v78, s[98:99]
	s_add_u32 s98, s98, 0x100000
	s_addc_u32 s99, s99, 0
	s_waitcnt vmcnt(31)
	v_cvt_pk_bf16_f32 v83, v8, v9
	v_pk_fma_f32 v[8:9], v[4:5], v[8:9], v[36:37]
	global_store_dword v79, v83, s[100:101]
	s_add_u32 s100, s100, 0x80000
	s_addc_u32 s101, s101, 0
	global_load_dwordx2 v[36:37], v78, s[98:99]
	s_add_u32 s98, s98, 0x100000
	s_addc_u32 s99, s99, 0
	s_waitcnt vmcnt(31)
	v_cvt_pk_bf16_f32 v80, v8, v9
	v_pk_fma_f32 v[8:9], v[4:5], v[8:9], v[38:39]
	global_store_dword v79, v80, s[100:101]
	s_add_u32 s100, s100, 0x80000
	s_addc_u32 s101, s101, 0
	global_load_dwordx2 v[38:39], v78, s[98:99]
	s_add_u32 s98, s98, 0x100000
	s_addc_u32 s99, s99, 0
	s_waitcnt vmcnt(31)
	v_cvt_pk_bf16_f32 v81, v8, v9
	v_pk_fma_f32 v[8:9], v[4:5], v[8:9], v[40:41]
	global_store_dword v79, v81, s[100:101]
	s_add_u32 s100, s100, 0x80000
	s_addc_u32 s101, s101, 0
	global_load_dwordx2 v[40:41], v78, s[98:99]
	s_add_u32 s98, s98, 0x100000
	s_addc_u32 s99, s99, 0
	s_waitcnt vmcnt(31)
	v_cvt_pk_bf16_f32 v82, v8, v9
	v_pk_fma_f32 v[8:9], v[4:5], v[8:9], v[42:43]
	global_store_dword v79, v82, s[100:101]
	s_add_u32 s100, s100, 0x80000
	s_addc_u32 s101, s101, 0
	global_load_dwordx2 v[42:43], v78, s[98:99]
	s_add_u32 s98, s98, 0x100000
	s_addc_u32 s99, s99, 0
	s_waitcnt vmcnt(31)
	v_cvt_pk_bf16_f32 v83, v8, v9
	v_pk_fma_f32 v[8:9], v[4:5], v[8:9], v[44:45]
	global_store_dword v79, v83, s[100:101]
	s_add_u32 s100, s100, 0x80000
	s_addc_u32 s101, s101, 0
	global_load_dwordx2 v[44:45], v78, s[98:99]
	s_add_u32 s98, s98, 0x100000
	s_addc_u32 s99, s99, 0
	s_waitcnt vmcnt(31)
	v_cvt_pk_bf16_f32 v80, v8, v9
	v_pk_fma_f32 v[8:9], v[4:5], v[8:9], v[46:47]
	global_store_dword v79, v80, s[100:101]
	s_add_u32 s100, s100, 0x80000
	s_addc_u32 s101, s101, 0
	global_load_dwordx2 v[46:47], v78, s[98:99]
	s_add_u32 s98, s98, 0x100000
	s_addc_u32 s99, s99, 0
	s_waitcnt vmcnt(31)
	v_cvt_pk_bf16_f32 v81, v8, v9
	v_pk_fma_f32 v[8:9], v[4:5], v[8:9], v[48:49]
	global_store_dword v79, v81, s[100:101]
	s_add_u32 s100, s100, 0x80000
	s_addc_u32 s101, s101, 0
	global_load_dwordx2 v[48:49], v78, s[98:99]
	s_add_u32 s98, s98, 0x100000
	s_addc_u32 s99, s99, 0
	s_waitcnt vmcnt(31)
	v_cvt_pk_bf16_f32 v82, v8, v9
	v_pk_fma_f32 v[8:9], v[4:5], v[8:9], v[50:51]
	global_store_dword v79, v82, s[100:101]
	s_add_u32 s100, s100, 0x80000
	s_addc_u32 s101, s101, 0
	global_load_dwordx2 v[50:51], v78, s[98:99]
	s_add_u32 s98, s98, 0x100000
	s_addc_u32 s99, s99, 0
	s_waitcnt vmcnt(31)
	v_cvt_pk_bf16_f32 v83, v8, v9
	v_pk_fma_f32 v[8:9], v[4:5], v[8:9], v[52:53]
	global_store_dword v79, v83, s[100:101]
	s_add_u32 s100, s100, 0x80000
	s_addc_u32 s101, s101, 0
	global_load_dwordx2 v[52:53], v78, s[98:99]
	s_add_u32 s98, s98, 0x100000
	s_addc_u32 s99, s99, 0
	s_waitcnt vmcnt(31)
	v_cvt_pk_bf16_f32 v80, v8, v9
	v_pk_fma_f32 v[8:9], v[4:5], v[8:9], v[54:55]
	global_store_dword v79, v80, s[100:101]
	s_add_u32 s100, s100, 0x80000
	s_addc_u32 s101, s101, 0
	global_load_dwordx2 v[54:55], v78, s[98:99]
	s_add_u32 s98, s98, 0x100000
	s_addc_u32 s99, s99, 0
	s_waitcnt vmcnt(31)
	v_cvt_pk_bf16_f32 v81, v8, v9
	v_pk_fma_f32 v[8:9], v[4:5], v[8:9], v[56:57]
	global_store_dword v79, v81, s[100:101]
	s_add_u32 s100, s100, 0x80000
	s_addc_u32 s101, s101, 0
	global_load_dwordx2 v[56:57], v78, s[98:99]
	s_add_u32 s98, s98, 0x100000
	s_addc_u32 s99, s99, 0
	s_waitcnt vmcnt(31)
	v_cvt_pk_bf16_f32 v82, v8, v9
	v_pk_fma_f32 v[8:9], v[4:5], v[8:9], v[58:59]
	global_store_dword v79, v82, s[100:101]
	s_add_u32 s100, s100, 0x80000
	s_addc_u32 s101, s101, 0
	global_load_dwordx2 v[58:59], v78, s[98:99]
	s_add_u32 s98, s98, 0x100000
	s_addc_u32 s99, s99, 0
	s_waitcnt vmcnt(31)
	v_cvt_pk_bf16_f32 v83, v8, v9
	v_pk_fma_f32 v[8:9], v[4:5], v[8:9], v[60:61]
	global_store_dword v79, v83, s[100:101]
	s_add_u32 s100, s100, 0x80000
	s_addc_u32 s101, s101, 0
	global_load_dwordx2 v[60:61], v78, s[98:99]
	s_add_u32 s98, s98, 0x100000
	s_addc_u32 s99, s99, 0
	s_waitcnt vmcnt(31)
	v_cvt_pk_bf16_f32 v80, v8, v9
	v_pk_fma_f32 v[8:9], v[4:5], v[8:9], v[62:63]
	global_store_dword v79, v80, s[100:101]
	s_add_u32 s100, s100, 0x80000
	s_addc_u32 s101, s101, 0
	global_load_dwordx2 v[62:63], v78, s[98:99]
	s_add_u32 s98, s98, 0x100000
	s_addc_u32 s99, s99, 0
	s_waitcnt vmcnt(31)
	v_cvt_pk_bf16_f32 v81, v8, v9
	v_pk_fma_f32 v[8:9], v[4:5], v[8:9], v[64:65]
	global_store_dword v79, v81, s[100:101]
	s_add_u32 s100, s100, 0x80000
	s_addc_u32 s101, s101, 0
	global_load_dwordx2 v[64:65], v78, s[98:99]
	s_add_u32 s98, s98, 0x100000
	s_addc_u32 s99, s99, 0
	s_waitcnt vmcnt(31)
	v_cvt_pk_bf16_f32 v82, v8, v9
	v_pk_fma_f32 v[8:9], v[4:5], v[8:9], v[66:67]
	global_store_dword v79, v82, s[100:101]
	s_add_u32 s100, s100, 0x80000
	s_addc_u32 s101, s101, 0
	global_load_dwordx2 v[66:67], v78, s[98:99]
	s_add_u32 s98, s98, 0x100000
	s_addc_u32 s99, s99, 0
	s_waitcnt vmcnt(31)
	v_cvt_pk_bf16_f32 v83, v8, v9
	v_pk_fma_f32 v[8:9], v[4:5], v[8:9], v[68:69]
	global_store_dword v79, v83, s[100:101]
	s_add_u32 s100, s100, 0x80000
	s_addc_u32 s101, s101, 0
	global_load_dwordx2 v[68:69], v78, s[98:99]
	s_add_u32 s98, s98, 0x100000
	s_addc_u32 s99, s99, 0
	s_waitcnt vmcnt(31)
	v_cvt_pk_bf16_f32 v80, v8, v9
	v_pk_fma_f32 v[8:9], v[4:5], v[8:9], v[70:71]
	global_store_dword v79, v80, s[100:101]
	s_add_u32 s100, s100, 0x80000
	s_addc_u32 s101, s101, 0
	global_load_dwordx2 v[70:71], v78, s[98:99]
	s_add_u32 s98, s98, 0x100000
	s_addc_u32 s99, s99, 0
	s_waitcnt vmcnt(31)
	v_cvt_pk_bf16_f32 v81, v8, v9
	v_pk_fma_f32 v[8:9], v[4:5], v[8:9], v[72:73]
	global_store_dword v79, v81, s[100:101]
	s_add_u32 s100, s100, 0x80000
	s_addc_u32 s101, s101, 0
	global_load_dwordx2 v[72:73], v78, s[98:99]
	s_add_u32 s98, s98, 0x100000
	s_addc_u32 s99, s99, 0
	s_waitcnt vmcnt(31)
	v_cvt_pk_bf16_f32 v82, v8, v9
	v_pk_fma_f32 v[8:9], v[4:5], v[8:9], v[74:75]
	global_store_dword v79, v82, s[100:101]
	s_add_u32 s100, s100, 0x80000
	s_addc_u32 s101, s101, 0
	global_load_dwordx2 v[74:75], v78, s[98:99]
	s_add_u32 s98, s98, 0x100000
	s_addc_u32 s99, s99, 0
	s_waitcnt vmcnt(31)
	v_cvt_pk_bf16_f32 v83, v8, v9
	v_pk_fma_f32 v[8:9], v[4:5], v[8:9], v[76:77]
	global_store_dword v79, v83, s[100:101]
	s_add_u32 s100, s100, 0x80000
	s_addc_u32 s101, s101, 0
	global_load_dwordx2 v[76:77], v78, s[98:99]
	s_add_u32 s98, s98, 0x100000
	s_addc_u32 s99, s99, 0
	s_waitcnt vmcnt(31)
	v_cvt_pk_bf16_f32 v80, v8, v9
	v_pk_fma_f32 v[8:9], v[4:5], v[8:9], v[14:15]
	global_store_dword v79, v80, s[100:101]
	s_add_u32 s100, s100, 0x80000
	s_addc_u32 s101, s101, 0
	s_waitcnt vmcnt(30)
	v_cvt_pk_bf16_f32 v81, v8, v9
	v_pk_fma_f32 v[8:9], v[4:5], v[8:9], v[16:17]
	global_store_dword v79, v81, s[100:101]
	s_add_u32 s100, s100, 0x80000
	s_addc_u32 s101, s101, 0
	s_waitcnt vmcnt(29)
	v_cvt_pk_bf16_f32 v82, v8, v9
	v_pk_fma_f32 v[8:9], v[4:5], v[8:9], v[18:19]
	global_store_dword v79, v82, s[100:101]
	s_add_u32 s100, s100, 0x80000
	s_addc_u32 s101, s101, 0
	s_waitcnt vmcnt(28)
	v_cvt_pk_bf16_f32 v83, v8, v9
	v_pk_fma_f32 v[8:9], v[4:5], v[8:9], v[20:21]
	global_store_dword v79, v83, s[100:101]
	s_add_u32 s100, s100, 0x80000
	s_addc_u32 s101, s101, 0
	s_waitcnt vmcnt(27)
	v_cvt_pk_bf16_f32 v80, v8, v9
	v_pk_fma_f32 v[8:9], v[4:5], v[8:9], v[22:23]
	global_store_dword v79, v80, s[100:101]
	s_add_u32 s100, s100, 0x80000
	s_addc_u32 s101, s101, 0
	s_waitcnt vmcnt(26)
	v_cvt_pk_bf16_f32 v81, v8, v9
	v_pk_fma_f32 v[8:9], v[4:5], v[8:9], v[24:25]
	global_store_dword v79, v81, s[100:101]
	s_add_u32 s100, s100, 0x80000
	s_addc_u32 s101, s101, 0
	s_waitcnt vmcnt(25)
	v_cvt_pk_bf16_f32 v82, v8, v9
	v_pk_fma_f32 v[8:9], v[4:5], v[8:9], v[26:27]
	global_store_dword v79, v82, s[100:101]
	s_add_u32 s100, s100, 0x80000
	s_addc_u32 s101, s101, 0
	s_waitcnt vmcnt(24)
	v_cvt_pk_bf16_f32 v83, v8, v9
	v_pk_fma_f32 v[8:9], v[4:5], v[8:9], v[28:29]
	global_store_dword v79, v83, s[100:101]
	s_add_u32 s100, s100, 0x80000
	s_addc_u32 s101, s101, 0
	s_waitcnt vmcnt(23)
	v_cvt_pk_bf16_f32 v80, v8, v9
	v_pk_fma_f32 v[8:9], v[4:5], v[8:9], v[30:31]
	global_store_dword v79, v80, s[100:101]
	s_add_u32 s100, s100, 0x80000
	s_addc_u32 s101, s101, 0
	s_waitcnt vmcnt(22)
	v_cvt_pk_bf16_f32 v81, v8, v9
	v_pk_fma_f32 v[8:9], v[4:5], v[8:9], v[32:33]
	global_store_dword v79, v81, s[100:101]
	s_add_u32 s100, s100, 0x80000
	s_addc_u32 s101, s101, 0
	s_waitcnt vmcnt(21)
	v_cvt_pk_bf16_f32 v82, v8, v9
	v_pk_fma_f32 v[8:9], v[4:5], v[8:9], v[34:35]
	global_store_dword v79, v82, s[100:101]
	s_add_u32 s100, s100, 0x80000
	s_addc_u32 s101, s101, 0
	s_waitcnt vmcnt(20)
	v_cvt_pk_bf16_f32 v83, v8, v9
	v_pk_fma_f32 v[8:9], v[4:5], v[8:9], v[36:37]
	global_store_dword v79, v83, s[100:101]
	s_add_u32 s100, s100, 0x80000
	s_addc_u32 s101, s101, 0
	s_waitcnt vmcnt(19)
	v_cvt_pk_bf16_f32 v80, v8, v9
	v_pk_fma_f32 v[8:9], v[4:5], v[8:9], v[38:39]
	global_store_dword v79, v80, s[100:101]
	s_add_u32 s100, s100, 0x80000
	s_addc_u32 s101, s101, 0
	s_waitcnt vmcnt(18)
	v_cvt_pk_bf16_f32 v81, v8, v9
	v_pk_fma_f32 v[8:9], v[4:5], v[8:9], v[40:41]
	global_store_dword v79, v81, s[100:101]
	s_add_u32 s100, s100, 0x80000
	s_addc_u32 s101, s101, 0
	s_waitcnt vmcnt(17)
	v_cvt_pk_bf16_f32 v82, v8, v9
	v_pk_fma_f32 v[8:9], v[4:5], v[8:9], v[42:43]
	global_store_dword v79, v82, s[100:101]
	s_add_u32 s100, s100, 0x80000
	s_addc_u32 s101, s101, 0
	s_waitcnt vmcnt(16)
	v_cvt_pk_bf16_f32 v83, v8, v9
	v_pk_fma_f32 v[8:9], v[4:5], v[8:9], v[44:45]
	global_store_dword v79, v83, s[100:101]
	s_add_u32 s100, s100, 0x80000
	s_addc_u32 s101, s101, 0
	s_waitcnt vmcnt(15)
	v_cvt_pk_bf16_f32 v80, v8, v9
	v_pk_fma_f32 v[8:9], v[4:5], v[8:9], v[46:47]
	global_store_dword v79, v80, s[100:101]
	s_add_u32 s100, s100, 0x80000
	s_addc_u32 s101, s101, 0
	s_waitcnt vmcnt(14)
	v_cvt_pk_bf16_f32 v81, v8, v9
	v_pk_fma_f32 v[8:9], v[4:5], v[8:9], v[48:49]
	global_store_dword v79, v81, s[100:101]
	s_add_u32 s100, s100, 0x80000
	s_addc_u32 s101, s101, 0
	s_waitcnt vmcnt(13)
	v_cvt_pk_bf16_f32 v82, v8, v9
	v_pk_fma_f32 v[8:9], v[4:5], v[8:9], v[50:51]
	global_store_dword v79, v82, s[100:101]
	s_add_u32 s100, s100, 0x80000
	s_addc_u32 s101, s101, 0
	s_waitcnt vmcnt(12)
	v_cvt_pk_bf16_f32 v83, v8, v9
	v_pk_fma_f32 v[8:9], v[4:5], v[8:9], v[52:53]
	global_store_dword v79, v83, s[100:101]
	s_add_u32 s100, s100, 0x80000
	s_addc_u32 s101, s101, 0
	s_waitcnt vmcnt(11)
	v_cvt_pk_bf16_f32 v80, v8, v9
	v_pk_fma_f32 v[8:9], v[4:5], v[8:9], v[54:55]
	global_store_dword v79, v80, s[100:101]
	s_add_u32 s100, s100, 0x80000
	s_addc_u32 s101, s101, 0
	s_waitcnt vmcnt(10)
	v_cvt_pk_bf16_f32 v81, v8, v9
	v_pk_fma_f32 v[8:9], v[4:5], v[8:9], v[56:57]
	global_store_dword v79, v81, s[100:101]
	s_add_u32 s100, s100, 0x80000
	s_addc_u32 s101, s101, 0
	s_waitcnt vmcnt(9)
	v_cvt_pk_bf16_f32 v82, v8, v9
	v_pk_fma_f32 v[8:9], v[4:5], v[8:9], v[58:59]
	global_store_dword v79, v82, s[100:101]
	s_add_u32 s100, s100, 0x80000
	s_addc_u32 s101, s101, 0
	s_waitcnt vmcnt(8)
	v_cvt_pk_bf16_f32 v83, v8, v9
	v_pk_fma_f32 v[8:9], v[4:5], v[8:9], v[60:61]
	global_store_dword v79, v83, s[100:101]
	s_add_u32 s100, s100, 0x80000
	s_addc_u32 s101, s101, 0
	s_waitcnt vmcnt(7)
	v_cvt_pk_bf16_f32 v80, v8, v9
	v_pk_fma_f32 v[8:9], v[4:5], v[8:9], v[62:63]
	global_store_dword v79, v80, s[100:101]
	s_add_u32 s100, s100, 0x80000
	s_addc_u32 s101, s101, 0
	s_waitcnt vmcnt(6)
	v_cvt_pk_bf16_f32 v81, v8, v9
	v_pk_fma_f32 v[8:9], v[4:5], v[8:9], v[64:65]
	global_store_dword v79, v81, s[100:101]
	s_add_u32 s100, s100, 0x80000
	s_addc_u32 s101, s101, 0
	s_waitcnt vmcnt(5)
	v_cvt_pk_bf16_f32 v82, v8, v9
	v_pk_fma_f32 v[8:9], v[4:5], v[8:9], v[66:67]
	global_store_dword v79, v82, s[100:101]
	s_add_u32 s100, s100, 0x80000
	s_addc_u32 s101, s101, 0
	s_waitcnt vmcnt(4)
	v_cvt_pk_bf16_f32 v83, v8, v9
	v_pk_fma_f32 v[8:9], v[4:5], v[8:9], v[68:69]
	global_store_dword v79, v83, s[100:101]
	s_add_u32 s100, s100, 0x80000
	s_addc_u32 s101, s101, 0
	s_waitcnt vmcnt(3)
	v_cvt_pk_bf16_f32 v80, v8, v9
	v_pk_fma_f32 v[8:9], v[4:5], v[8:9], v[70:71]
	global_store_dword v79, v80, s[100:101]
	s_add_u32 s100, s100, 0x80000
	s_addc_u32 s101, s101, 0
	s_waitcnt vmcnt(2)
	v_cvt_pk_bf16_f32 v81, v8, v9
	v_pk_fma_f32 v[8:9], v[4:5], v[8:9], v[72:73]
	global_store_dword v79, v81, s[100:101]
	s_add_u32 s100, s100, 0x80000
	s_addc_u32 s101, s101, 0
	s_waitcnt vmcnt(1)
	v_cvt_pk_bf16_f32 v82, v8, v9
	v_pk_fma_f32 v[8:9], v[4:5], v[8:9], v[74:75]
	global_store_dword v79, v82, s[100:101]
	s_add_u32 s100, s100, 0x80000
	s_addc_u32 s101, s101, 0
	s_waitcnt vmcnt(0)
	v_cvt_pk_bf16_f32 v83, v8, v9
	v_pk_fma_f32 v[8:9], v[4:5], v[8:9], v[76:77]
	global_store_dword v79, v83, s[100:101]
	s_add_u32 s100, s100, 0x80000
	s_addc_u32 s101, s101, 0
	v_add_u32_e32 v1, s14, v1
	v_cmp_lt_i32_e32 vcc, s20, v1
	s_or_b64 s[8:9], vcc, s[8:9]
	v_add_u32_e32 v10, s15, v10
	s_andn2_b64 exec, exec, s[8:9]
	s_cbranch_execnz .LBB0_870
